# attention merge: previous log-sum-exp loaded by 16 lanes and broadcast with ds_bpermute instead of a 64-lane load with 4 identical addresses per row
# baseline (speedup 1.0000x reference)
; __device__ __forceinline__ float opaque_f(float c) { float v = c; asm volatile("" : "+s"(v)); return v; }
; __device__ __forceinline__ void attn_group_mfma5(const bf16* QK, const float* bias2g, int ldil, int first, bf16* OACC, float* LSE, LAS unsigned char* lds, const int tid, const int bid, const int G) {
;     ...
;     const int wq = __builtin_amdgcn_readfirstlane(tid >> 6), lane = tid & 63, n = lane & 15, kq = lane >> 4;
;     const int Ls = SEQ >> ldil, lq4 = 4 - ldil, nq4m = (1 << lq4) - 1, dilm = (1 << ldil) - 1;
;     constexpr float SC = 0.125f * 1.4426950409f;
;     const float NEGBIG = opaque_f(-1e30f);
;     constexpr int NP = BATCH * HA * 16 / 2;
;     const int npp = (NP + G - 1) / G, ns = 2 * npp;
;     const bool remap = (G == 256);
;     constexpr int AT5_BUF = 2 * 32768 + 768;
; __global__ void __launch_bounds__(NTHREADS, 2) mk_fwd(Args args) {
;     ...
;             const int ldil = 2 * aux;
;             if (ldil < 4 && G * 8 == BATCH * HA * 16 / 2) attn_group_ring(P_BIG, P_BIAS + aux * 16 * 129, ldil, aux == 0, P_OACC, P_LSE, lds + RING_OFF, tid, bid, G);
;             else attn_group_mfma5(P_BIG, P_BIAS + aux * 16 * 129, ldil, aux == 0, P_OACC, P_LSE, lds + RING_OFF, tid, bid, G);
.LBB0_149:
	s_and_b64 vcc, exec, s[2:3]
	s_cbranch_vccz .LBB0_268
	s_lshl_b32 s43, s24, 1
	s_cmp_lt_u32 s24, 2
	s_cselect_b64 s[0:1], -1, 0
	s_cmpk_eq_i32 s88, 0x100
	s_cselect_b64 s[10:11], -1, 0
	s_cmpk_lg_i32 s88, 0x100
	s_cselect_b64 s[12:13], -1, 0
	s_and_b64 s[0:1], s[0:1], s[10:11]
	s_add_u32 s80, s96, 0xda00000
	v_mbcnt_lo_u32_b32 v69, -1, 0
	v_mbcnt_hi_u32_b32 v69, -1, v69
	s_addc_u32 s81, s97, 0
	v_add_u32_e32 v68, s30, v69
	s_mov_b64 s[2:3], -1
	s_andn2_b64 vcc, exec, s[0:1]
	s_waitcnt vmcnt(0)
	v_and_b32_e32 v66, 63, v69
	v_and_b32_e32 v67, 15, v69
	v_bfe_u32 v51, v69, 4, 2
	v_and_b32_e32 v112, 1, v51
	v_mul_u32_u24_e32 v112, 24, v112
	v_mov_b32_e32 v113, 0
	v_lshlrev_b32_e32 v116, 2, v67
	s_cbranch_vccz .LBB0_225
	s_mul_i32 s60, s24, 0x810
	s_lshl_b64 s[0:1], s[60:61], 2
	s_add_u32 s0, s96, s0
	s_addc_u32 s1, s97, s1
	s_add_u32 s14, s0, 0x140000
	s_addc_u32 s15, s1, 0
	s_abs_i32 s2, s88
	v_cvt_f32_u32_e32 v0, s2
	v_readfirstlane_b32 s0, v68
	s_sub_i32 s39, 4, s43
	s_ashr_i32 s1, s0, 6
	v_rcp_iflag_f32_e32 v0, v0
	s_lshl_b32 s0, -1, s39
	s_sub_i32 s4, 0, s2
	s_not_b32 s48, s0
	v_mul_f32_e32 v0, 0x4f7ffffe, v0
	v_cvt_u32_f32_e32 v0, v0
	s_lshl_b32 s0, -1, s43
	s_not_b32 s49, s0
	s_add_i32 s0, s88, 0x7ff
	v_readfirstlane_b32 s5, v0
	s_mul_i32 s4, s4, s5
	s_mul_hi_u32 s4, s5, s4
	s_xor_b32 s3, s0, s88
	s_abs_i32 s0, s0
	s_add_i32 s5, s5, s4
	s_mul_hi_u32 s4, s0, s5
	s_mul_i32 s5, s4, s2
	s_sub_i32 s0, s0, s5
	s_lshr_b32 s33, 0x800, s43
	s_ashr_i32 s3, s3, 31
	s_add_i32 s5, s4, 1
	s_sub_i32 s6, s0, s2
	s_cmp_ge_u32 s0, s2
	s_cselect_b32 s4, s5, s4
	s_cselect_b32 s0, s6, s0
	s_add_i32 s5, s4, 1
	s_cmp_ge_u32 s0, s2
	s_cselect_b32 s0, s5, s4
	s_xor_b32 s0, s0, s3
	s_sub_i32 s40, s0, s3
	s_cmp_gt_i32 s40, 0
	s_mov_b32 s50, 0xf149f2ca
	s_cselect_b64 s[2:3], -1, 0
	s_cmp_lt_i32 s40, 1
	s_cbranch_scc1 .LBB0_165
	s_mov_b64 s[4:5], -1
	s_and_b64 vcc, exec, s[12:13]
	s_cbranch_vccz .LBB0_154
	s_mul_i32 s0, s40, s90
	s_cbranch_execnz .LBB0_156
	s_branch .LBB0_155

; #define LAS __attribute__((address_space(3)))
; #define AT_SU(s_) (2 * AT_P((s_) >> 1) + ((s_) & 1))
; #define AT_FETCH_Q(su_) do { const int su__ = (su_); const bf16* qp_ = QK + ((((size_t)((su__ >> 8) * 16 + ((su__ >> 4) & 15)) << ldil) | ((su__ >> lq4) & dilm)) * Ls + ((su__ & nq4m) * 128 + 16 * wq + n)) * 64 + 8 * kq; \
;         qf[0] = *(const bf16x8s*)qp_; qf[1] = *(const bf16x8s*)(qp_ + 32); } while (0)
; #define AT_SU(s_) (2 * AT_P((s_) >> 1) + ((s_) & 1))
; #define AT_FETCH_Q(su_) do { const int su__ = (su_); const bf16* qp_ = QK + ((((size_t)((su__ >> 8) * 16 + ((su__ >> 4) & 15)) << ldil) | ((su__ >> lq4) & dilm)) * Ls + ((su__ & nq4m) * 128 + 16 * wq + n)) * 64 + 8 * kq; \
;         qf[0] = *(const bf16x8s*)qp_; qf[1] = *(const bf16x8s*)(qp_ + 32); tick += 2; } while (0)
; __device__ __forceinline__ void attn_group_mfma5(const bf16* QK, const float* bias2g, int ldil, int first, bf16* OACC, float* LSE, LAS unsigned char* lds, const int tid, const int bid, const int G) {
;     ...
;         const int su = AT_SU(s), q4 = su & nq4m, rr = (su >> lq4) & dilm, h = (su >> 4) & 15, b = su >> 8;
;         const LAS unsigned char* Kl = lds + (s & 1) * AT5_BUF; const LAS unsigned char* Vl = Kl + 32768; const LAS float* tab = (const LAS float*)(Kl + 65536);
;         const size_t rowq = (size_t)b * SEQ + ((size_t)(q4 * 128 + 16 * wq + n) << ldil) + rr;
;         f32x4 S[9];
; #pragma unroll
;         for (int kb = 0; kb < 9; ++kb) S[kb] = (f32x4){0.f, 0.f, 0.f, 0.f};
;         { const LAS unsigned char* kp0 = Kl + (16 * wq + n) * 128;
; #pragma unroll
;           for (int ks = 0; ks < 2; ++ks)
; #pragma unroll
;             for (int kb = 0; kb < 9; ++kb) S[kb] = __builtin_amdgcn_mfma_f32_16x16x32_bf16(*(const LAS bf16x8s*)(kp0 + 16 * kb * 128 + (((4 * ks + kq) ^ fl) * 16)), qf[ks], S[kb], 0, 0, 0); }
;         __builtin_amdgcn_sched_barrier(0);
;         if (more) AT_FETCH_Q(AT_SU(s + 1));
;         float lold = 0.f; v2u xo[4];
;         if (!first) { lold = LSE[rowq * 16 + h];
; #pragma unroll
;             for (int db = 0; db < 4; ++db) xo[db] = *(const v2u*)(OACC + rowq * D + h * 64 + 16 * db + 4 * kq); }
.LBB0_215:
	s_lshl_b32 s0, s42, 1
	s_or_b32 s0, s0, s36
	s_and_b32 s36, s0, s48
	s_ashr_i32 s8, s42, 7
	s_ashr_i32 s0, s0, s39
	s_ashr_i32 s9, s8, 31
	s_lshl_b32 s36, s36, 7
	s_and_b32 s0, s0, s49
	s_lshl_b64 s[8:9], s[8:9], 11
	v_add_u32_e32 v0, s36, v71
	v_ashrrev_i32_e32 v1, 31, v0
	s_add_u32 s8, s8, s0
	s_addc_u32 s9, s9, 0
	v_lshlrev_b64 v[0:1], s43, v[0:1]
	v_lshl_add_u64 v[0:1], s[8:9], 0, v[0:1]
	v_cndmask_b32_e64 v2, 0, 1, s[44:45]
	v_lshlrev_b64 v[52:53], 6, v[0:1]
	v_lshlrev_b64 v[0:1], 11, v[0:1]
	s_bfe_u32 s0, s42, 0x40003
	v_cmp_ne_u32_e64 s[8:9], 1, v2
	s_andn2_b64 vcc, exec, s[44:45]
	v_lshl_add_u64 v[62:63], s[52:53], 0, v[52:53]
	v_lshl_add_u64 v[60:61], s[46:47], 0, v[0:1]
	v_lshlrev_b32_e32 v58, 1, v50
	s_cbranch_vccnz .LBB0_217
	s_lshl_b32 s60, s0, 2
	v_lshl_add_u64 v[0:1], v[62:63], 0, s[60:61]
	s_lshl_b32 s60, s0, 7
	v_lshl_add_u64 v[52:53], v[60:61], 0, s[60:61]
	v_mov_b32_e32 v59, v3
	v_lshl_add_u64 v[52:53], v[52:53], 0, v[58:59]
	v_lshl_add_u64 v[114:115], v[52:53], 0, v[112:113]
	s_mov_b64 s[98:99], exec
	s_mov_b64 exec, 0xffff
	global_load_dword v59, v[0:1], off
	s_mov_b64 exec, s[98:99]
	global_load_dwordx4 v[104:107], v[114:115], off
	global_load_dwordx4 v[108:111], v[114:115], off offset:64
	s_branch .LBB0_218

; #define LAS __attribute__((address_space(3)))
; template <int O> __device__ __forceinline__ float swz_xor(float v) { return __builtin_bit_cast(float, __builtin_amdgcn_ds_swizzle(__builtin_bit_cast(int, v), (O << 10) | 0x1f)); }
; __device__ __forceinline__ float get_xor32(float v, int lane) { return __builtin_bit_cast(float, __builtin_amdgcn_ds_bpermute((lane ^ 32) << 2, __builtin_bit_cast(int, v))); }
; __device__ __forceinline__ void attn_group_mfma5(const bf16* QK, const float* bias2g, int ldil, int first, bf16* OACC, float* LSE, LAS unsigned char* lds, const int tid, const int bid, const int G) {
;     ...
;         const LAS float* tb = tab + (32 + 4 * kq - n);
;         int kt0 = q4 * 128 - 64 + 16 * wq + 4 * kq; asm volatile("" : "+v"(kt0));
;         float mx = NEGBIG;
; #pragma unroll
;         for (int kb = 0; kb < 9; ++kb)
; #pragma unroll
;             for (int e = 0; e < 4; ++e) { const int krel = 16 * kb + e;
;                 float sv = S[kb][e] * SC + tb[krel]; sv = ((unsigned)(kt0 + krel) >= (unsigned)Ls) ? NEGBIG : sv; S[kb][e] = sv; mx = fmaxf(mx, sv); }
;         mx = fmaxf(mx, swz_xor<16>(mx)); mx = fmaxf(mx, get_xor32(mx, lane));
.LBB0_218:
	v_lshl_add_u32 v0, v73, 2, s1
	v_add_u32_e32 v84, 0x10080, v0
	v_add_u32_e32 v2, s36, v74
	ds_read2_b32 v[0:1], v84 offset1:1
	ds_read2_b32 v[86:87], v84 offset0:2 offset1:3
	v_cmp_gt_u32_e32 vcc, s33, v2
	s_waitcnt lgkmcnt(0)
	v_fmamk_f32 v0, v44, 0x3e38aa3b, v0
	v_mov_b32_e32 v44, s50
	v_fmac_f32_e32 v1, 0x3e38aa3b, v45
	v_add_u32_e32 v45, 1, v2
	v_cndmask_b32_e32 v0, v44, v0, vcc
	v_cmp_gt_u32_e32 vcc, s33, v45
	v_fmamk_f32 v45, v46, 0x3e38aa3b, v86
	v_add_u32_e32 v46, 2, v2
	v_cndmask_b32_e32 v1, v44, v1, vcc
	v_cmp_gt_u32_e32 vcc, s33, v46
	v_add_u32_e32 v46, 3, v2
	v_fmac_f32_e32 v87, 0x3e38aa3b, v47
	v_cndmask_b32_e32 v45, v44, v45, vcc
	v_cmp_gt_u32_e32 vcc, s33, v46
	v_max3_f32 v85, s50, v0, v1
	s_nop 0
	v_cndmask_b32_e32 v46, v44, v87, vcc
	ds_read2_b32 v[86:87], v84 offset0:16 offset1:17
	v_max3_f32 v47, v85, v45, v46
	v_add_u32_e32 v85, 16, v2
	v_cmp_gt_u32_e32 vcc, s33, v85
	v_add_u32_e32 v85, 18, v2
	s_waitcnt lgkmcnt(0)
	v_fmamk_f32 v40, v40, 0x3e38aa3b, v86
	v_fmac_f32_e32 v87, 0x3e38aa3b, v41
	v_add_u32_e32 v41, 17, v2
	v_cndmask_b32_e32 v40, v44, v40, vcc
	v_cmp_gt_u32_e32 vcc, s33, v41
	s_nop 1
	v_cndmask_b32_e32 v41, v44, v87, vcc
	ds_read2_b32 v[86:87], v84 offset0:18 offset1:19
	v_cmp_gt_u32_e32 vcc, s33, v85
	v_add_u32_e32 v85, 32, v2
	v_max3_f32 v47, v47, v40, v41
	s_waitcnt lgkmcnt(0)
	v_fmamk_f32 v42, v42, 0x3e38aa3b, v86
	v_fmac_f32_e32 v87, 0x3e38aa3b, v43
	v_add_u32_e32 v43, 19, v2
	v_cndmask_b32_e32 v42, v44, v42, vcc
	v_cmp_gt_u32_e32 vcc, s33, v43
	s_nop 1
	v_cndmask_b32_e32 v43, v44, v87, vcc
	ds_read2_b32 v[86:87], v84 offset0:32 offset1:33
	v_cmp_gt_u32_e32 vcc, s33, v85
	v_add_u32_e32 v85, 34, v2
	v_max3_f32 v47, v47, v42, v43
	s_waitcnt lgkmcnt(0)
	v_fmamk_f32 v36, v36, 0x3e38aa3b, v86
	v_fmac_f32_e32 v87, 0x3e38aa3b, v37
	v_add_u32_e32 v37, 33, v2
	v_cndmask_b32_e32 v36, v44, v36, vcc
	v_cmp_gt_u32_e32 vcc, s33, v37
	s_nop 1
	v_cndmask_b32_e32 v37, v44, v87, vcc
	ds_read2_b32 v[86:87], v84 offset0:34 offset1:35
	v_cmp_gt_u32_e32 vcc, s33, v85
	v_add_u32_e32 v85, 48, v2
	v_max3_f32 v47, v47, v36, v37
	s_waitcnt lgkmcnt(0)
	v_fmamk_f32 v38, v38, 0x3e38aa3b, v86
	v_fmac_f32_e32 v87, 0x3e38aa3b, v39
	v_add_u32_e32 v39, 35, v2
	v_cndmask_b32_e32 v38, v44, v38, vcc
	v_cmp_gt_u32_e32 vcc, s33, v39
	s_nop 1
	v_cndmask_b32_e32 v39, v44, v87, vcc
	ds_read2_b32 v[86:87], v84 offset0:48 offset1:49
	v_cmp_gt_u32_e32 vcc, s33, v85
	v_add_u32_e32 v85, 50, v2
	v_max3_f32 v47, v47, v38, v39
	s_waitcnt lgkmcnt(0)
	v_fmamk_f32 v32, v32, 0x3e38aa3b, v86
	v_fmac_f32_e32 v87, 0x3e38aa3b, v33
	v_add_u32_e32 v33, 49, v2
	v_cndmask_b32_e32 v32, v44, v32, vcc
	v_cmp_gt_u32_e32 vcc, s33, v33
	s_nop 1
	v_cndmask_b32_e32 v33, v44, v87, vcc
	ds_read2_b32 v[86:87], v84 offset0:50 offset1:51
	v_cmp_gt_u32_e32 vcc, s33, v85
	v_add_u32_e32 v85, 64, v2
	v_max3_f32 v47, v47, v32, v33
	s_waitcnt lgkmcnt(0)
	v_fmamk_f32 v34, v34, 0x3e38aa3b, v86
	v_fmac_f32_e32 v87, 0x3e38aa3b, v35
	v_add_u32_e32 v35, 51, v2
	v_cndmask_b32_e32 v34, v44, v34, vcc
	v_cmp_gt_u32_e32 vcc, s33, v35
	s_nop 1
	v_cndmask_b32_e32 v35, v44, v87, vcc
	ds_read2_b32 v[86:87], v84 offset0:64 offset1:65
	v_cmp_gt_u32_e32 vcc, s33, v85
	v_max3_f32 v47, v47, v34, v35
	s_waitcnt lgkmcnt(0)
	v_fmamk_f32 v28, v28, 0x3e38aa3b, v86
	v_fmac_f32_e32 v87, 0x3e38aa3b, v29
	v_add_u32_e32 v29, 0x41, v2
	v_cndmask_b32_e32 v28, v44, v28, vcc
	v_cmp_gt_u32_e32 vcc, s33, v29
	s_nop 1
	v_cndmask_b32_e32 v29, v44, v87, vcc
	ds_read2_b32 v[86:87], v84 offset0:66 offset1:67
	v_max3_f32 v85, v47, v28, v29
	v_add_u32_e32 v47, 0x42, v2
	v_cmp_gt_u32_e32 vcc, s33, v47
	s_waitcnt lgkmcnt(0)
	v_fmamk_f32 v30, v30, 0x3e38aa3b, v86
	v_cndmask_b32_e32 v47, v44, v30, vcc
	v_add_u32_e32 v30, 0x43, v2
	v_fmac_f32_e32 v87, 0x3e38aa3b, v31
	v_cmp_gt_u32_e32 vcc, s33, v30
	s_nop 1
	v_cndmask_b32_e32 v31, v44, v87, vcc
	ds_read2_b32 v[86:87], v84 offset0:80 offset1:81
	v_max3_f32 v30, v85, v47, v31
	v_add_u32_e32 v85, 0x50, v2
	v_cmp_gt_u32_e32 vcc, s33, v85
	v_add_u32_e32 v85, 0x52, v2
	s_waitcnt lgkmcnt(0)
	v_fmamk_f32 v24, v24, 0x3e38aa3b, v86
	v_fmac_f32_e32 v87, 0x3e38aa3b, v25
	v_add_u32_e32 v25, 0x51, v2
	v_cndmask_b32_e32 v24, v44, v24, vcc
	v_cmp_gt_u32_e32 vcc, s33, v25
	s_nop 1
	v_cndmask_b32_e32 v25, v44, v87, vcc
	ds_read2_b32 v[86:87], v84 offset0:82 offset1:83
	v_cmp_gt_u32_e32 vcc, s33, v85
	v_max3_f32 v30, v30, v24, v25
	s_waitcnt lgkmcnt(0)
	v_fmamk_f32 v26, v26, 0x3e38aa3b, v86
	v_cndmask_b32_e32 v85, v44, v26, vcc
	v_add_u32_e32 v26, 0x53, v2
	v_fmac_f32_e32 v87, 0x3e38aa3b, v27
	v_cmp_gt_u32_e32 vcc, s33, v26
	ds_read2_b32 v[26:27], v84 offset0:96 offset1:97
	s_waitcnt lgkmcnt(0)
	v_fmamk_f32 v20, v20, 0x3e38aa3b, v26
	v_add_u32_e32 v26, 0x60, v2
	v_cndmask_b32_e32 v86, v44, v87, vcc
	v_cmp_gt_u32_e32 vcc, s33, v26
	v_fmac_f32_e32 v27, 0x3e38aa3b, v21
	v_max3_f32 v30, v30, v85, v86
	v_cndmask_b32_e32 v26, v44, v20, vcc
	v_add_u32_e32 v20, 0x61, v2
	v_cmp_gt_u32_e32 vcc, s33, v20
	ds_read2_b32 v[20:21], v84 offset0:98 offset1:99
	s_waitcnt lgkmcnt(0)
	v_fmamk_f32 v20, v22, 0x3e38aa3b, v20
	v_add_u32_e32 v22, 0x62, v2
	v_cndmask_b32_e32 v27, v44, v27, vcc
	v_cmp_gt_u32_e32 vcc, s33, v22
	v_fmac_f32_e32 v21, 0x3e38aa3b, v23
	v_max3_f32 v30, v30, v26, v27
	v_cndmask_b32_e32 v87, v44, v20, vcc
	v_add_u32_e32 v20, 0x63, v2
	v_cmp_gt_u32_e32 vcc, s33, v20
	s_nop 1
	v_cndmask_b32_e32 v88, v44, v21, vcc
	ds_read2_b32 v[20:21], v84 offset0:112 offset1:113
	v_max3_f32 v22, v30, v87, v88
	s_waitcnt lgkmcnt(0)
	v_fmamk_f32 v16, v16, 0x3e38aa3b, v20
	v_add_u32_e32 v20, 0x70, v2
	v_cmp_gt_u32_e32 vcc, s33, v20
	v_fmac_f32_e32 v21, 0x3e38aa3b, v17
	s_nop 0
	v_cndmask_b32_e32 v89, v44, v16, vcc
	v_add_u32_e32 v16, 0x71, v2
	v_cmp_gt_u32_e32 vcc, s33, v16
	ds_read2_b32 v[16:17], v84 offset0:114 offset1:115
	s_waitcnt lgkmcnt(0)
; template <int O> __device__ __forceinline__ float swz_xor(float v) { return __builtin_bit_cast(float, __builtin_amdgcn_ds_swizzle(__builtin_bit_cast(int, v), (O << 10) | 0x1f)); }
; __device__ __forceinline__ void attn_group_mfma5(const bf16* QK, const float* bias2g, int ldil, int first, bf16* OACC, float* LSE, LAS unsigned char* lds, const int tid, const int bid, const int G) {
;     ...
;         mx = fmaxf(mx, swz_xor<16>(mx)); mx = fmaxf(mx, get_xor32(mx, lane));
;         float l = 0.f; v4u pb[5];
; #pragma unroll
;         for (int kb = 0; kb < 9; ++kb) {
;             const float p0 = __builtin_amdgcn_exp2f(S[kb][0] - mx), p1 = __builtin_amdgcn_exp2f(S[kb][1] - mx), p2 = __builtin_amdgcn_exp2f(S[kb][2] - mx), p3 = __builtin_amdgcn_exp2f(S[kb][3] - mx);
;             l += (p0 + p1) + (p2 + p3);
;             if (kb & 1) { pb[kb >> 1].z = cvtpk(p0, p1); pb[kb >> 1].w = cvtpk(p2, p3); } else { pb[kb >> 1].x = cvtpk(p0, p1); pb[kb >> 1].y = cvtpk(p2, p3); } }
;         pb[4].z = 0u; pb[4].w = 0u;
;         l += swz_xor<16>(l); l += get_xor32(l, lane);
;         f32x4 O[4];
; #pragma unroll
;         for (int db = 0; db < 4; ++db) O[db] = (f32x4){0.f, 0.f, 0.f, 0.f};
;         { const int vf = (2 * kq + (n >> 3)) & 7;
;           const unsigned vb0 = (unsigned)(size_t)(Vl + (16 * wq + 4 * kq + (n >> 2)) * 128 + 8 * (n & 1));
;           unsigned ad[4];
; #pragma unroll
;           for (int db = 0; db < 4; ++db) ad[db] = vb0 + (unsigned)(((2 * db + ((n & 3) >> 1)) ^ vf) * 16);
; #pragma unroll
;           for (int t = 0; t < 5; ++t) {
;               v2u l0, l1, l2, l3, h0 = (v2u){0u, 0u}, h1 = h0, h2 = h0, h3 = h0;
;               if (t < 4) asm volatile("ds_read_b64_tr_b16 %0, %8 offset:%12\n\tds_read_b64_tr_b16 %1, %9 offset:%12\n\tds_read_b64_tr_b16 %2, %10 offset:%12\n\tds_read_b64_tr_b16 %3, %11 offset:%12\n\t"
;                                       "ds_read_b64_tr_b16 %4, %8 offset:%13\n\tds_read_b64_tr_b16 %5, %9 offset:%13\n\tds_read_b64_tr_b16 %6, %10 offset:%13\n\tds_read_b64_tr_b16 %7, %11 offset:%13\n\ts_waitcnt lgkmcnt(0)"
;                                       : "=&v"(l0), "=&v"(l1), "=&v"(l2), "=&v"(l3), "=&v"(h0), "=&v"(h1), "=&v"(h2), "=&v"(h3) : "v"(ad[0]), "v"(ad[1]), "v"(ad[2]), "v"(ad[3]), "n"(t * 4096), "n"(t * 4096 + 2048) : "memory");
	v_fmamk_f32 v16, v18, 0x3e38aa3b, v16
	v_add_u32_e32 v18, 0x72, v2
	v_cndmask_b32_e32 v90, v44, v21, vcc
	v_cmp_gt_u32_e32 vcc, s33, v18
	v_fmac_f32_e32 v17, 0x3e38aa3b, v19
	v_max3_f32 v20, v22, v89, v90
	v_cndmask_b32_e32 v91, v44, v16, vcc
	v_add_u32_e32 v16, 0x73, v2
	v_cmp_gt_u32_e32 vcc, s33, v16
	s_nop 1
	v_cndmask_b32_e32 v92, v44, v17, vcc
	ds_read2_b32 v[16:17], v84 offset0:128 offset1:129
	v_max3_f32 v18, v20, v91, v92
	s_waitcnt lgkmcnt(0)
	v_fmamk_f32 v12, v12, 0x3e38aa3b, v16
	v_add_u32_e32 v16, 0x80, v2
	v_cmp_gt_u32_e32 vcc, s33, v16
	v_fmac_f32_e32 v17, 0x3e38aa3b, v13
	s_nop 0
	v_cndmask_b32_e32 v93, v44, v12, vcc
	v_add_u32_e32 v12, 0x81, v2
	v_cmp_gt_u32_e32 vcc, s33, v12
	ds_read2_b32 v[12:13], v84 offset0:130 offset1:131
	s_waitcnt lgkmcnt(0)
	v_fmamk_f32 v12, v14, 0x3e38aa3b, v12
	v_add_u32_e32 v14, 0x82, v2
	v_cndmask_b32_e32 v94, v44, v17, vcc
	v_cmp_gt_u32_e32 vcc, s33, v14
	v_add_u32_e32 v2, 0x83, v2
	v_fmac_f32_e32 v13, 0x3e38aa3b, v15
	v_cndmask_b32_e32 v84, v44, v12, vcc
	v_cmp_gt_u32_e32 vcc, s33, v2
	v_max3_f32 v16, v18, v93, v94
	s_nop 0
	v_cndmask_b32_e32 v44, v44, v13, vcc
	v_max3_f32 v2, v16, v84, v44
	v_mov_b32_e32 v12, v2
	s_nop 1
	v_permlane16_swap_b32_e32 v12, v2
	s_and_b64 vcc, exec, s[8:9]
	s_waitcnt lgkmcnt(0)
	v_max_f32_e32 v12, v12, v12
	v_max_f32_e32 v2, v2, v12
	v_mov_b32_e32 v12, v2
	s_nop 1
	v_permlane32_swap_b32_e32 v12, v2
	s_waitcnt lgkmcnt(0)
	v_max_f32_e32 v12, v12, v12
	v_max_f32_e32 v30, v2, v12
	v_sub_f32_e32 v1, v1, v30
	v_sub_f32_e32 v0, v0, v30
	v_exp_f32_e32 v12, v1
	v_sub_f32_e32 v1, v45, v30
	v_sub_f32_e32 v2, v46, v30
	v_exp_f32_e32 v0, v0
	v_exp_f32_e32 v1, v1
	v_exp_f32_e32 v13, v2
	s_nop 0
	v_pk_add_f32 v[14:15], v[0:1], v[12:13]
	v_cvt_pk_bf16_f32 v13, v1, v13
	v_sub_f32_e32 v1, v41, v30
	v_cvt_pk_bf16_f32 v12, v0, v12
	v_sub_f32_e32 v0, v40, v30
	v_exp_f32_e32 v2, v1
	v_sub_f32_e32 v1, v42, v30
	v_pk_add_f32 v[18:19], v[14:15], v[14:15] op_sel_hi:[0,1]
	v_exp_f32_e32 v0, v0
	v_exp_f32_e32 v15, v1
	v_sub_f32_e32 v1, v43, v30
	v_exp_f32_e32 v16, v1
	v_add_f32_e32 v1, v0, v2
	v_cvt_pk_bf16_f32 v14, v0, v2
	v_sub_f32_e32 v2, v37, v30
	v_add_f32_e32 v17, v15, v16
	v_cvt_pk_bf16_f32 v15, v15, v16
	v_sub_f32_e32 v0, v36, v30
	v_exp_f32_e32 v16, v2
	v_sub_f32_e32 v2, v38, v30
	v_exp_f32_e32 v0, v0
	v_exp_f32_e32 v18, v2
	v_sub_f32_e32 v2, v39, v30
	v_exp_f32_e32 v2, v2
	v_pk_add_f32 v[20:21], v[0:1], v[16:17]
	v_sub_f32_e32 v1, v33, v30
	v_cvt_pk_bf16_f32 v16, v0, v16
	v_pk_add_f32 v[22:23], v[18:19], v[2:3]
	v_cvt_pk_bf16_f32 v17, v18, v2
	v_sub_f32_e32 v0, v32, v30
	v_exp_f32_e32 v18, v1
	v_sub_f32_e32 v1, v34, v30
	v_sub_f32_e32 v2, v35, v30
	v_exp_f32_e32 v0, v0
	v_exp_f32_e32 v1, v1
	v_exp_f32_e32 v19, v2
	v_pk_add_f32 v[20:21], v[20:21], v[22:23]
	s_nop 0
	v_pk_add_f32 v[36:37], v[20:21], v[20:21] op_sel_hi:[0,1]
	v_pk_add_f32 v[20:21], v[0:1], v[18:19]
	v_cvt_pk_bf16_f32 v19, v1, v19
	v_sub_f32_e32 v1, v29, v30
	v_cvt_pk_bf16_f32 v18, v0, v18
	v_sub_f32_e32 v0, v28, v30
	v_exp_f32_e32 v2, v1
	v_sub_f32_e32 v1, v47, v30
	v_pk_add_f32 v[32:33], v[20:21], v[20:21] op_sel_hi:[0,1]
	v_exp_f32_e32 v0, v0
	v_exp_f32_e32 v21, v1
	v_sub_f32_e32 v1, v31, v30
	v_exp_f32_e32 v22, v1
	v_add_f32_e32 v1, v0, v2
	v_cvt_pk_bf16_f32 v20, v0, v2
	v_sub_f32_e32 v2, v25, v30
	v_add_f32_e32 v23, v21, v22
	v_cvt_pk_bf16_f32 v21, v21, v22
	v_exp_f32_e32 v22, v2
	v_sub_f32_e32 v2, v85, v30
	v_sub_f32_e32 v0, v24, v30
	v_exp_f32_e32 v32, v2
	v_sub_f32_e32 v2, v86, v30
	v_exp_f32_e32 v0, v0
	v_exp_f32_e32 v36, v2
	v_sub_f32_e32 v2, v88, v30
	v_add_u32_e32 v31, s1, v76
	v_pk_add_f32 v[24:25], v[0:1], v[22:23]
	v_pk_add_f32 v[28:29], v[32:33], v[36:37]
	v_sub_f32_e32 v1, v27, v30
	v_pk_add_f32 v[24:25], v[24:25], v[28:29]
	v_cvt_pk_bf16_f32 v22, v0, v22
	v_pk_add_f32 v[28:29], v[24:25], v[24:25] op_sel_hi:[0,1]
	v_sub_f32_e32 v0, v26, v30
	v_exp_f32_e32 v24, v1
	v_sub_f32_e32 v1, v87, v30
	v_exp_f32_e32 v0, v0
	v_exp_f32_e32 v1, v1
	v_exp_f32_e32 v25, v2
	v_cvt_pk_bf16_f32 v23, v32, v36
	s_mov_b32 s1, 0x8000
	v_add3_u32 v31, v31, v77, s1
	v_pk_add_f32 v[26:27], v[0:1], v[24:25]
	v_cvt_pk_bf16_f32 v24, v0, v24
	v_cvt_pk_bf16_f32 v25, v1, v25
	v_sub_f32_e32 v0, v89, v30
	v_sub_f32_e32 v1, v90, v30
	v_exp_f32_e32 v0, v0
	v_exp_f32_e32 v2, v1
	v_sub_f32_e32 v1, v91, v30
	v_pk_add_f32 v[32:33], v[26:27], v[26:27] op_sel_hi:[0,1]
	v_exp_f32_e32 v27, v1
	v_sub_f32_e32 v1, v92, v30
	v_exp_f32_e32 v28, v1
	v_add_f32_e32 v1, v0, v2
	v_cvt_pk_bf16_f32 v26, v0, v2
	v_sub_f32_e32 v2, v94, v30
	v_exp_f32_e32 v34, v2
	v_sub_f32_e32 v2, v84, v30
	v_sub_f32_e32 v0, v93, v30
	v_exp_f32_e32 v32, v2
	v_sub_f32_e32 v2, v44, v30
	v_add_f32_e32 v35, v27, v28
	v_cvt_pk_bf16_f32 v27, v27, v28
	v_exp_f32_e32 v0, v0
	v_exp_f32_e32 v28, v2
	v_add_u32_e32 v96, v80, v31
	v_add_u32_e32 v97, v81, v31
	v_pk_add_f32 v[36:37], v[0:1], v[34:35]
	v_pk_add_f32 v[38:39], v[32:33], v[28:29]
	v_cvt_pk_bf16_f32 v0, v0, v34
	v_pk_add_f32 v[36:37], v[36:37], v[38:39]
	v_cvt_pk_bf16_f32 v1, v32, v28
	v_add_f32_e32 v29, v36, v37
	v_add_u32_e32 v98, v82, v31
	v_add_u32_e32 v31, v83, v31
	ds_read_b64_tr_b16 v[44:45], v96 offset:0
	ds_read_b64_tr_b16 v[40:41], v97 offset:0
	ds_read_b64_tr_b16 v[36:37], v98 offset:0
	ds_read_b64_tr_b16 v[32:33], v31 offset:0
	ds_read_b64_tr_b16 v[46:47], v96 offset:0x800
	ds_read_b64_tr_b16 v[42:43], v97 offset:0x800
	ds_read_b64_tr_b16 v[38:39], v98 offset:0x800
	ds_read_b64_tr_b16 v[34:35], v31 offset:0x800
	s_waitcnt lgkmcnt(0)
; __device__ __forceinline__ void attn_group_mfma5(const bf16* QK, const float* bias2g, int ldil, int first, bf16* OACC, float* LSE, LAS unsigned char* lds, const int tid, const int bid, const int G) {
;     ...
;           for (int t = 0; t < 5; ++t) {
;               v2u l0, l1, l2, l3, h0 = (v2u){0u, 0u}, h1 = h0, h2 = h0, h3 = h0;
;               if (t < 4) asm volatile("ds_read_b64_tr_b16 %0, %8 offset:%12\n\tds_read_b64_tr_b16 %1, %9 offset:%12\n\tds_read_b64_tr_b16 %2, %10 offset:%12\n\tds_read_b64_tr_b16 %3, %11 offset:%12\n\t"
;                                       "ds_read_b64_tr_b16 %4, %8 offset:%13\n\tds_read_b64_tr_b16 %5, %9 offset:%13\n\tds_read_b64_tr_b16 %6, %10 offset:%13\n\tds_read_b64_tr_b16 %7, %11 offset:%13\n\ts_waitcnt lgkmcnt(0)"
;                                       : "=&v"(l0), "=&v"(l1), "=&v"(l2), "=&v"(l3), "=&v"(h0), "=&v"(h1), "=&v"(h2), "=&v"(h3) : "v"(ad[0]), "v"(ad[1]), "v"(ad[2]), "v"(ad[3]), "n"(t * 4096), "n"(t * 4096 + 2048) : "memory");
;               else asm volatile("ds_read_b64_tr_b16 %0, %4 offset:%8\n\tds_read_b64_tr_b16 %1, %5 offset:%8\n\tds_read_b64_tr_b16 %2, %6 offset:%8\n\tds_read_b64_tr_b16 %3, %7 offset:%8\n\ts_waitcnt lgkmcnt(0)"
;                                 : "=&v"(l0), "=&v"(l1), "=&v"(l2), "=&v"(l3) : "v"(ad[0]), "v"(ad[1]), "v"(ad[2]), "v"(ad[3]), "n"(t * 4096) : "memory");
;               const bf16x8s pf = __builtin_bit_cast(bf16x8s, pb[t]);
;               O[0] = __builtin_amdgcn_mfma_f32_16x16x32_bf16(__builtin_bit_cast(bf16x8s, ((v4u){l0.x, l0.y, h0.x, h0.y})), pf, O[0], 0, 0, 0);
;               O[1] = __builtin_amdgcn_mfma_f32_16x16x32_bf16(__builtin_bit_cast(bf16x8s, ((v4u){l1.x, l1.y, h1.x, h1.y})), pf, O[1], 0, 0, 0);
;               O[2] = __builtin_amdgcn_mfma_f32_16x16x32_bf16(__builtin_bit_cast(bf16x8s, ((v4u){l2.x, l2.y, h2.x, h2.y})), pf, O[2], 0, 0, 0);
;               O[3] = __builtin_amdgcn_mfma_f32_16x16x32_bf16(__builtin_bit_cast(bf16x8s, ((v4u){l3.x, l3.y, h3.x, h3.y})), pf, O[3], 0, 0, 0); } }
;         const float il = __builtin_amdgcn_rcpf(l); float lse = mx + __builtin_amdgcn_logf(l);
;         float wn = il, wo = 0.f;
;         if (!first) { const float mm = fmaxf(lold, lse), eo = __builtin_amdgcn_exp2f(lold - mm), en = __builtin_amdgcn_exp2f(lse - mm), inv = __builtin_amdgcn_rcpf(eo + en); wn = en * inv * il; wo = eo * inv; lse = mm + __builtin_amdgcn_logf(eo + en); }
	v_mov_b32_e32 v2, v3
	v_mfma_f32_16x16x32_bf16 v[36:39], v[36:39], v[12:15], 0
	v_mov_b32_e32 v28, v29
	s_nop 1
	v_permlane16_swap_b32_e32 v28, v29
	s_waitcnt lgkmcnt(0)
	v_add_f32_e32 v28, v29, v28
	v_mfma_f32_16x16x32_bf16 v[44:47], v[44:47], v[12:15], 0
	v_mov_b32_e32 v29, v28
	s_nop 1
	v_permlane32_swap_b32_e32 v29, v28
	v_mfma_f32_16x16x32_bf16 v[40:43], v[40:43], v[12:15], 0
	v_mfma_f32_16x16x32_bf16 v[12:15], v[32:35], v[12:15], 0
	ds_read_b64_tr_b16 v[92:93], v96 offset:0x1000
	ds_read_b64_tr_b16 v[88:89], v97 offset:0x1000
	ds_read_b64_tr_b16 v[84:85], v98 offset:0x1000
	ds_read_b64_tr_b16 v[32:33], v31 offset:0x1000
	ds_read_b64_tr_b16 v[94:95], v96 offset:0x1800
	ds_read_b64_tr_b16 v[90:91], v97 offset:0x1800
	ds_read_b64_tr_b16 v[86:87], v98 offset:0x1800
	ds_read_b64_tr_b16 v[34:35], v31 offset:0x1800
	s_waitcnt lgkmcnt(0)
	s_nop 0
	v_mfma_f32_16x16x32_bf16 v[36:39], v[84:87], v[16:19], v[36:39]
	v_mfma_f32_16x16x32_bf16 v[44:47], v[92:95], v[16:19], v[44:47]
	v_mfma_f32_16x16x32_bf16 v[40:43], v[88:91], v[16:19], v[40:43]
	v_mfma_f32_16x16x32_bf16 v[12:15], v[32:35], v[16:19], v[12:15]
	ds_read_b64_tr_b16 v[88:89], v96 offset:0x2000
	ds_read_b64_tr_b16 v[84:85], v97 offset:0x2000
	ds_read_b64_tr_b16 v[32:33], v98 offset:0x2000
	ds_read_b64_tr_b16 v[16:17], v31 offset:0x2000
	ds_read_b64_tr_b16 v[90:91], v96 offset:0x2800
	ds_read_b64_tr_b16 v[86:87], v97 offset:0x2800
	ds_read_b64_tr_b16 v[34:35], v98 offset:0x2800
	ds_read_b64_tr_b16 v[18:19], v31 offset:0x2800
	s_waitcnt lgkmcnt(0)
	s_nop 0
	v_mfma_f32_16x16x32_bf16 v[32:35], v[32:35], v[20:23], v[36:39]
	v_mfma_f32_16x16x32_bf16 v[44:47], v[88:91], v[20:23], v[44:47]
	v_mfma_f32_16x16x32_bf16 v[40:43], v[84:87], v[20:23], v[40:43]
	v_mfma_f32_16x16x32_bf16 v[12:15], v[16:19], v[20:23], v[12:15]
	ds_read_b64_tr_b16 v[84:85], v96 offset:0x3000
	ds_read_b64_tr_b16 v[36:37], v97 offset:0x3000
	ds_read_b64_tr_b16 v[20:21], v98 offset:0x3000
	ds_read_b64_tr_b16 v[16:17], v31 offset:0x3000
	ds_read_b64_tr_b16 v[86:87], v96 offset:0x3800
	ds_read_b64_tr_b16 v[38:39], v97 offset:0x3800
	ds_read_b64_tr_b16 v[22:23], v98 offset:0x3800
	ds_read_b64_tr_b16 v[18:19], v31 offset:0x3800
	s_waitcnt lgkmcnt(0)
	s_nop 0
	v_mfma_f32_16x16x32_bf16 v[32:35], v[20:23], v[24:27], v[32:35]
	v_mov_b32_e32 v22, v3
	v_mov_b32_e32 v23, v3
	v_mfma_f32_16x16x32_bf16 v[44:47], v[84:87], v[24:27], v[44:47]
	v_mfma_f32_16x16x32_bf16 v[36:39], v[36:39], v[24:27], v[40:43]
	v_mfma_f32_16x16x32_bf16 v[12:15], v[16:19], v[24:27], v[12:15]
	ds_read_b64_tr_b16 v[20:21], v96 offset:0x4000
	ds_read_b64_tr_b16 v[18:19], v97 offset:0x4000
	ds_read_b64_tr_b16 v[16:17], v98 offset:0x4000
	ds_read_b64_tr_b16 v[40:41], v31 offset:0x4000
	s_waitcnt lgkmcnt(0)
	s_nop 1
	v_mov_b32_e32 v42, v3
	v_mov_b32_e32 v43, v3
	v_mfma_f32_16x16x32_bf16 v[24:27], v[20:23], v[0:3], v[44:47]
	v_mov_b32_e32 v20, v3
	v_mov_b32_e32 v21, v3
	v_mfma_f32_16x16x32_bf16 v[12:15], v[40:43], v[0:3], v[12:15]
	s_nop 0
	v_mfma_f32_16x16x32_bf16 v[20:23], v[18:21], v[0:3], v[36:39]
	v_mov_b32_e32 v18, v3
	v_mov_b32_e32 v19, v3
	s_nop 1
	v_mfma_f32_16x16x32_bf16 v[16:19], v[16:19], v[0:3], v[32:35]
	s_waitcnt lgkmcnt(0)
	v_add_f32_e32 v1, v28, v29
	v_rcp_f32_e32 v0, v1
	v_log_f32_e32 v1, v1
	s_nop 0
	v_add_f32_e32 v28, v30, v1
	s_cbranch_vccnz .LBB0_223
	v_max_f32_e32 v1, v28, v28
	s_waitcnt vmcnt(0)
	ds_bpermute_b32 v59, v116, v59
	s_waitcnt lgkmcnt(0)
	v_max_f32_e32 v2, v59, v59
	v_max_f32_e32 v2, v2, v1
	v_sub_f32_e32 v1, v59, v2
	v_sub_f32_e32 v28, v28, v2
	v_exp_f32_e32 v1, v1
	v_exp_f32_e32 v28, v28
	s_nop 0
	v_add_f32_e32 v30, v1, v28
	v_rcp_f32_e32 v29, v30
	v_log_f32_e32 v30, v30
	v_mul_f32_e32 v28, v28, v29
	v_pk_mul_f32 v[0:1], v[0:1], v[28:29]
	v_add_f32_e32 v28, v2, v30
	v_mov_b32_e32 v2, v1
	s_and_saveexec_b64 s[8:9], s[4:5]
	s_cbranch_execz .LBB0_221

; #define LAS __attribute__((address_space(3)))
; #define AT_SU(s_) (2 * AT_P((s_) >> 1) + ((s_) & 1))
; #define AT_FETCH_Q(su_) do { const int su__ = (su_); const bf16* qp_ = QK + ((((size_t)((su__ >> 8) * 16 + ((su__ >> 4) & 15)) << ldil) | ((su__ >> lq4) & dilm)) * Ls + ((su__ & nq4m) * 128 + 16 * wq + n)) * 64 + 8 * kq; \
;         qf[0] = *(const bf16x8s*)qp_; qf[1] = *(const bf16x8s*)(qp_ + 32); } while (0)
; #define AT_SU(s_) (2 * AT_P((s_) >> 1) + ((s_) & 1))
; #define AT_FETCH_Q(su_) do { const int su__ = (su_); const bf16* qp_ = QK + ((((size_t)((su__ >> 8) * 16 + ((su__ >> 4) & 15)) << ldil) | ((su__ >> lq4) & dilm)) * Ls + ((su__ & nq4m) * 128 + 16 * wq + n)) * 64 + 8 * kq; \
;         qf[0] = *(const bf16x8s*)qp_; qf[1] = *(const bf16x8s*)(qp_ + 32); tick += 2; } while (0)
; __device__ __forceinline__ void attn_group_ring(const bf16* QK, const float* bias2g, int ldil, int first, bf16* OACC, float* LSE, LAS unsigned char* lds, const int tid, const int bid, const int G) {
;     ...
;         const int su = AT_SU(s), q4 = su & nq4m, rr = (su >> lq4) & dilm, h = (su >> 4) & 15, b = su >> 8;
;         const size_t rowq = (size_t)b * SEQ + ((size_t)(q4 * 128 + 16 * wq + n) << ldil) + rr;
;         f32x4 S[9];
; #pragma unroll
;         for (int kb = 0; kb < 9; ++kb) S[kb] = (f32x4){0.f, 0.f, 0.f, 0.f};
; #pragma unroll
;         for (int ks = 0; ks < 2; ++ks)
; #pragma unroll
;             for (int kb = 0; kb < 9; ++kb) { const int wrow = 16 * (wq + kb);
;                 const LAS unsigned char* kp = lds + ((a + (wrow >> 7)) & 3) * 32768 + ((wrow & 127) + n) * 128 + (((4 * ks + kq) ^ fl) * 16);
;                 S[kb] = __builtin_amdgcn_mfma_f32_16x16x32_bf16(*(const LAS bf16x8s*)kp, qf[ks], S[kb], 0, 0, 0); }
;         __builtin_amdgcn_sched_barrier(0);
;         if (more) AT_FETCH_Q(AT_SU(s + 1));
;         float lold = 0.f; v2u xo[4];
;         if (!first) { lold = LSE[rowq * 16 + h];
; #pragma unroll
;             for (int db = 0; db < 4; ++db) xo[db] = *(const v2u*)(OACC + rowq * D + h * 64 + 16 * db + 4 * kq); }
.LBB0_240:
	s_bfe_u32 s1, s87, 0x20001
	s_cmp_lt_u32 s87, 8
	s_cselect_b64 s[4:5], -1, 0
	v_cndmask_b32_e64 v0, 0, 1, s[4:5]
	v_cndmask_b32_e64 v2, 0, 1, s[6:7]
	v_readfirstlane_b32 s4, v0
	s_or_b32 s4, s49, s4
	s_lshl_b32 s5, s4, 7
	s_or_b32 s1, s5, s1
	s_or_b32 s1, s1, s45
	s_lshl_b32 s1, s1, 1
	s_and_b32 s5, s87, 1
	s_or_b32 s1, s1, s5
	s_and_b32 s70, s1, s47
	s_ashr_i32 s1, s1, s14
	s_and_b32 s71, s1, s48
	s_lshl_b32 s1, s70, 7
	s_ashr_i32 s5, s4, 31
	v_add_u32_e32 v0, s1, v64
	s_lshl_b64 s[4:5], s[4:5], 11
	v_ashrrev_i32_e32 v1, 31, v0
	s_or_b32 s4, s4, s71
	v_lshlrev_b64 v[0:1], s43, v[0:1]
	v_lshl_add_u64 v[0:1], s[4:5], 0, v[0:1]
	v_lshlrev_b64 v[52:53], 6, v[0:1]
	v_lshlrev_b64 v[0:1], 11, v[0:1]
	v_cmp_ne_u32_e64 s[4:5], 1, v2
	s_andn2_b64 vcc, exec, s[6:7]
	v_lshl_add_u64 v[60:61], s[8:9], 0, v[52:53]
	v_lshl_add_u64 v[52:53], v[50:51], 0, v[0:1]
	v_lshl_add_u64 v[114:115], v[52:53], 0, v[112:113]
	s_cbranch_vccnz .LBB0_242
	s_mov_b64 s[98:99], exec
	s_mov_b64 exec, 0xffff
	global_load_dword v84, v[60:61], off
	s_mov_b64 exec, s[98:99]
	global_load_dwordx4 v[104:107], v[114:115], off
	global_load_dwordx4 v[108:111], v[114:115], off offset:64
	s_branch .LBB0_243

; #define LAS __attribute__((address_space(3)))
; template <int O> __device__ __forceinline__ float swz_xor(float v) { return __builtin_bit_cast(float, __builtin_amdgcn_ds_swizzle(__builtin_bit_cast(int, v), (O << 10) | 0x1f)); }
; __device__ __forceinline__ float get_xor32(float v, int lane) { return __builtin_bit_cast(float, __builtin_amdgcn_ds_bpermute((lane ^ 32) << 2, __builtin_bit_cast(int, v))); }
; __device__ __forceinline__ void attn_group_ring(const bf16* QK, const float* bias2g, int ldil, int first, bf16* OACC, float* LSE, LAS unsigned char* lds, const int tid, const int bid, const int G) {
;     ...
;         const LAS float* tb = tab + (32 + 4 * kq - n);
;         int kt0 = q4 * 128 - 64 + 16 * wq + 4 * kq; asm volatile("" : "+v"(kt0));
;         float mx = NEGBIG;
; #pragma unroll
;         for (int kb = 0; kb < 9; ++kb)
; #pragma unroll
;             for (int e = 0; e < 4; ++e) { const int krel = 16 * kb + e;
;                 float sv = S[kb][e] * SC + tb[krel]; sv = ((unsigned)(kt0 + krel) >= (unsigned)Ls) ? NEGBIG : sv; S[kb][e] = sv; mx = fmaxf(mx, sv); }
;         mx = fmaxf(mx, swz_xor<16>(mx)); mx = fmaxf(mx, get_xor32(mx, lane));
.LBB0_243:
	s_movk_i32 s70, 0xff
	s_movk_i32 s71, 0xdf
	v_add_u32_e32 v2, s1, v83
	ds_read2_b32 v[0:1], v65 offset0:32 offset1:33
	ds_read2_b32 v[86:87], v65 offset0:34 offset1:35
	v_cmp_gt_u32_e32 vcc, s13, v2
	s_add_i32 s1, s78, s87
	s_add_i32 s1, s1, s0
	s_waitcnt lgkmcnt(0)
	v_fmamk_f32 v0, v44, 0x3e38aa3b, v0
	v_mov_b32_e32 v44, s12
	v_fmac_f32_e32 v1, 0x3e38aa3b, v45
	v_add_u32_e32 v45, 1, v2
	v_cndmask_b32_e32 v0, v44, v0, vcc
	v_cmp_gt_u32_e32 vcc, s13, v45
	v_fmamk_f32 v45, v46, 0x3e38aa3b, v86
	v_add_u32_e32 v46, 2, v2
	v_cndmask_b32_e32 v1, v44, v1, vcc
	v_cmp_gt_u32_e32 vcc, s13, v46
	v_add_u32_e32 v46, 3, v2
	v_fmac_f32_e32 v87, 0x3e38aa3b, v47
	v_cndmask_b32_e32 v45, v44, v45, vcc
	v_cmp_gt_u32_e32 vcc, s13, v46
	v_max3_f32 v85, s12, v0, v1
	s_lshl_b32 s1, s1, 15
	v_cndmask_b32_e32 v46, v44, v87, vcc
	ds_read2_b32 v[86:87], v65 offset0:48 offset1:49
	v_max3_f32 v47, v85, v45, v46
	v_add_u32_e32 v85, 16, v2
	v_cmp_gt_u32_e32 vcc, s13, v85
	v_add_u32_e32 v85, 18, v2
	s_waitcnt lgkmcnt(0)
	v_fmamk_f32 v40, v40, 0x3e38aa3b, v86
	v_fmac_f32_e32 v87, 0x3e38aa3b, v41
	v_add_u32_e32 v41, 17, v2
	v_cndmask_b32_e32 v40, v44, v40, vcc
	v_cmp_gt_u32_e32 vcc, s13, v41
	s_and_b32 s1, s1, 0x18000
	s_add_i32 s1, s93, s1
	v_cndmask_b32_e32 v41, v44, v87, vcc
	ds_read2_b32 v[86:87], v65 offset0:50 offset1:51
	v_cmp_gt_u32_e32 vcc, s13, v85
	v_add_u32_e32 v85, 32, v2
	v_max3_f32 v47, v47, v40, v41
	s_addk_i32 s1, 0x4000
	s_waitcnt lgkmcnt(0)
	v_fmamk_f32 v42, v42, 0x3e38aa3b, v86
	v_fmac_f32_e32 v87, 0x3e38aa3b, v43
	v_add_u32_e32 v43, 19, v2
	v_cndmask_b32_e32 v42, v44, v42, vcc
	v_cmp_gt_u32_e32 vcc, s13, v43
	s_nop 1
	v_cndmask_b32_e32 v43, v44, v87, vcc
	ds_read2_b32 v[86:87], v65 offset0:64 offset1:65
	v_cmp_gt_u32_e32 vcc, s13, v85
	v_add_u32_e32 v85, 34, v2
	v_max3_f32 v47, v47, v42, v43
	s_waitcnt lgkmcnt(0)
	v_fmamk_f32 v36, v36, 0x3e38aa3b, v86
	v_fmac_f32_e32 v87, 0x3e38aa3b, v37
	v_add_u32_e32 v37, 33, v2
	v_cndmask_b32_e32 v36, v44, v36, vcc
	v_cmp_gt_u32_e32 vcc, s13, v37
	s_nop 1
	v_cndmask_b32_e32 v37, v44, v87, vcc
	ds_read2_b32 v[86:87], v65 offset0:66 offset1:67
	v_cmp_gt_u32_e32 vcc, s13, v85
	v_add_u32_e32 v85, 48, v2
	v_max3_f32 v47, v47, v36, v37
	s_waitcnt lgkmcnt(0)
	v_fmamk_f32 v38, v38, 0x3e38aa3b, v86
	v_fmac_f32_e32 v87, 0x3e38aa3b, v39
	v_add_u32_e32 v39, 35, v2
	v_cndmask_b32_e32 v38, v44, v38, vcc
	v_cmp_gt_u32_e32 vcc, s13, v39
	s_nop 1
	v_cndmask_b32_e32 v39, v44, v87, vcc
	ds_read2_b32 v[86:87], v65 offset0:80 offset1:81
	v_cmp_gt_u32_e32 vcc, s13, v85
	v_max3_f32 v47, v47, v38, v39
	s_waitcnt lgkmcnt(0)
	v_fmamk_f32 v32, v32, 0x3e38aa3b, v86
	v_fmac_f32_e32 v87, 0x3e38aa3b, v33
	v_add_u32_e32 v33, 49, v2
	v_cndmask_b32_e32 v32, v44, v32, vcc
	v_cmp_gt_u32_e32 vcc, s13, v33
	s_nop 1
	v_cndmask_b32_e32 v33, v44, v87, vcc
	ds_read2_b32 v[86:87], v65 offset0:82 offset1:83
	v_max3_f32 v85, v47, v32, v33
	v_add_u32_e32 v47, 50, v2
	v_cmp_gt_u32_e32 vcc, s13, v47
	s_waitcnt lgkmcnt(0)
	v_fmamk_f32 v34, v34, 0x3e38aa3b, v86
	v_cndmask_b32_e32 v47, v44, v34, vcc
	v_add_u32_e32 v34, 51, v2
	v_fmac_f32_e32 v87, 0x3e38aa3b, v35
	v_cmp_gt_u32_e32 vcc, s13, v34
	v_add_u32_e32 v34, 64, v2
	s_nop 0
	v_cndmask_b32_e32 v35, v44, v87, vcc
	ds_read2_b32 v[86:87], v65 offset0:96 offset1:97
	v_cmp_gt_u32_e32 vcc, s13, v34
	v_max3_f32 v85, v85, v47, v35
	s_waitcnt lgkmcnt(0)
	v_fmamk_f32 v28, v28, 0x3e38aa3b, v86
	v_cndmask_b32_e32 v34, v44, v28, vcc
	v_add_u32_e32 v28, 0x41, v2
	v_fmac_f32_e32 v87, 0x3e38aa3b, v29
	v_cmp_gt_u32_e32 vcc, s13, v28
	s_nop 1
	v_cndmask_b32_e32 v29, v44, v87, vcc
	ds_read2_b32 v[86:87], v65 offset0:98 offset1:99
	v_max3_f32 v28, v85, v34, v29
	v_add_u32_e32 v85, 0x42, v2
	v_cmp_gt_u32_e32 vcc, s13, v85
	v_add_u32_e32 v85, 0x50, v2
	s_waitcnt lgkmcnt(0)
	v_fmamk_f32 v30, v30, 0x3e38aa3b, v86
	v_fmac_f32_e32 v87, 0x3e38aa3b, v31
	v_add_u32_e32 v31, 0x43, v2
	v_cndmask_b32_e32 v30, v44, v30, vcc
	v_cmp_gt_u32_e32 vcc, s13, v31
	s_nop 1
	v_cndmask_b32_e32 v31, v44, v87, vcc
	ds_read2_b32 v[86:87], v65 offset0:112 offset1:113
	v_cmp_gt_u32_e32 vcc, s13, v85
	v_max3_f32 v28, v28, v30, v31
	s_waitcnt lgkmcnt(0)
	v_fmamk_f32 v24, v24, 0x3e38aa3b, v86
	v_cndmask_b32_e32 v85, v44, v24, vcc
	v_add_u32_e32 v24, 0x51, v2
	v_fmac_f32_e32 v87, 0x3e38aa3b, v25
	v_cmp_gt_u32_e32 vcc, s13, v24
	ds_read2_b32 v[24:25], v65 offset0:114 offset1:115
	s_waitcnt lgkmcnt(0)
	v_fmamk_f32 v24, v26, 0x3e38aa3b, v24
	v_add_u32_e32 v26, 0x52, v2
	v_cndmask_b32_e32 v86, v44, v87, vcc
	v_cmp_gt_u32_e32 vcc, s13, v26
	v_fmac_f32_e32 v25, 0x3e38aa3b, v27
	v_max3_f32 v28, v28, v85, v86
	v_cndmask_b32_e32 v89, v44, v24, vcc
	v_add_u32_e32 v24, 0x53, v2
	v_cmp_gt_u32_e32 vcc, s13, v24
	s_nop 1
	v_cndmask_b32_e32 v90, v44, v25, vcc
	ds_read2_b32 v[24:25], v65 offset0:128 offset1:129
	v_max3_f32 v26, v28, v89, v90
	s_waitcnt lgkmcnt(0)
	v_fmamk_f32 v20, v20, 0x3e38aa3b, v24
	v_add_u32_e32 v24, 0x60, v2
	v_cmp_gt_u32_e32 vcc, s13, v24
	v_fmac_f32_e32 v25, 0x3e38aa3b, v21
	s_nop 0
	v_cndmask_b32_e32 v87, v44, v20, vcc
	v_add_u32_e32 v20, 0x61, v2
	v_cmp_gt_u32_e32 vcc, s13, v20
	ds_read2_b32 v[20:21], v65 offset0:130 offset1:131
	s_waitcnt lgkmcnt(0)
	v_fmamk_f32 v20, v22, 0x3e38aa3b, v20
	v_add_u32_e32 v22, 0x62, v2
	v_cndmask_b32_e32 v88, v44, v25, vcc
	v_cmp_gt_u32_e32 vcc, s13, v22
	v_fmac_f32_e32 v21, 0x3e38aa3b, v23
	v_max3_f32 v24, v26, v87, v88
	v_cndmask_b32_e32 v91, v44, v20, vcc
	v_add_u32_e32 v20, 0x63, v2
	v_cmp_gt_u32_e32 vcc, s13, v20
	s_nop 1
	v_cndmask_b32_e32 v92, v44, v21, vcc
	ds_read2_b32 v[20:21], v65 offset0:144 offset1:145
	v_max3_f32 v22, v24, v91, v92
	s_waitcnt lgkmcnt(0)
; __device__ __forceinline__ void attn_group_ring(const bf16* QK, const float* bias2g, int ldil, int first, bf16* OACC, float* LSE, LAS unsigned char* lds, const int tid, const int bid, const int G) {
;     ...
;         mx = fmaxf(mx, swz_xor<16>(mx)); mx = fmaxf(mx, get_xor32(mx, lane));
;         float l = 0.f; v4u pb[5];
; #pragma unroll
;         for (int kb = 0; kb < 9; ++kb) {
;             const float p0 = __builtin_amdgcn_exp2f(S[kb][0] - mx), p1 = __builtin_amdgcn_exp2f(S[kb][1] - mx), p2 = __builtin_amdgcn_exp2f(S[kb][2] - mx), p3 = __builtin_amdgcn_exp2f(S[kb][3] - mx);
;             l += (p0 + p1) + (p2 + p3);
;             if (kb & 1) { pb[kb >> 1].z = cvtpk(p0, p1); pb[kb >> 1].w = cvtpk(p2, p3); } else { pb[kb >> 1].x = cvtpk(p0, p1); pb[kb >> 1].y = cvtpk(p2, p3); } }
;         pb[4].z = 0u; pb[4].w = 0u;
;         l += swz_xor<16>(l); l += get_xor32(l, lane);
;         f32x4 O[4];
; #pragma unroll
;         for (int db = 0; db < 4; ++db) O[db] = (f32x4){0.f, 0.f, 0.f, 0.f};
;         { const int vf = (2 * kq + (n >> 3)) & 7;
;           unsigned pcs[4];
; #pragma unroll
;           for (int db = 0; db < 4; ++db) pcs[db] = (unsigned)((4 * kq + (n >> 2)) * 128 + 8 * (n & 1) + (((2 * db + ((n & 3) >> 1)) ^ vf) * 16));
; #pragma unroll
;           for (int t = 0; t < 5; ++t) {
;               const int wlo = 16 * wq + 32 * t, whi = wlo + 16;
;               const unsigned blo = (unsigned)(size_t)(lds + ((a + (wlo >> 7)) & 3) * 32768 + 16384 + (wlo & 127) * 128), bhi = (unsigned)(size_t)(lds + ((a + (whi >> 7)) & 3) * 32768 + 16384 + (whi & 127) * 128);
;               v2u l0, l1, l2, l3, h0 = (v2u){0u, 0u}, h1 = h0, h2 = h0, h3 = h0;
;               const unsigned a0 = blo + pcs[0], a1 = blo + pcs[1], a2 = blo + pcs[2], a3 = blo + pcs[3];
;               if (t < 4) { const unsigned c0 = bhi + pcs[0], c1 = bhi + pcs[1], c2 = bhi + pcs[2], c3 = bhi + pcs[3];
;                   asm volatile("ds_read_b64_tr_b16 %0, %8\n\tds_read_b64_tr_b16 %1, %9\n\tds_read_b64_tr_b16 %2, %10\n\tds_read_b64_tr_b16 %3, %11\n\t"
;                                "ds_read_b64_tr_b16 %4, %12\n\tds_read_b64_tr_b16 %5, %13\n\tds_read_b64_tr_b16 %6, %14\n\tds_read_b64_tr_b16 %7, %15\n\ts_waitcnt lgkmcnt(0)"
	v_fmamk_f32 v16, v16, 0x3e38aa3b, v20
	v_add_u32_e32 v20, 0x70, v2
	v_cmp_gt_u32_e32 vcc, s13, v20
	v_fmac_f32_e32 v21, 0x3e38aa3b, v17
	s_nop 0
	v_cndmask_b32_e32 v93, v44, v16, vcc
	v_add_u32_e32 v16, 0x71, v2
	v_cmp_gt_u32_e32 vcc, s13, v16
	ds_read2_b32 v[16:17], v65 offset0:146 offset1:147
	s_waitcnt lgkmcnt(0)
	v_fmamk_f32 v16, v18, 0x3e38aa3b, v16
	v_add_u32_e32 v18, 0x72, v2
	v_cndmask_b32_e32 v94, v44, v21, vcc
	v_cmp_gt_u32_e32 vcc, s13, v18
	v_fmac_f32_e32 v17, 0x3e38aa3b, v19
	v_max3_f32 v20, v22, v93, v94
	v_cndmask_b32_e32 v95, v44, v16, vcc
	v_add_u32_e32 v16, 0x73, v2
	v_cmp_gt_u32_e32 vcc, s13, v16
	s_nop 1
	v_cndmask_b32_e32 v96, v44, v17, vcc
	ds_read2_b32 v[16:17], v65 offset0:160 offset1:161
	v_max3_f32 v18, v20, v95, v96
	s_waitcnt lgkmcnt(0)
	v_fmamk_f32 v12, v12, 0x3e38aa3b, v16
	v_add_u32_e32 v16, 0x80, v2
	v_cmp_gt_u32_e32 vcc, s13, v16
	v_fmac_f32_e32 v17, 0x3e38aa3b, v13
	s_nop 0
	v_cndmask_b32_e32 v97, v44, v12, vcc
	v_add_u32_e32 v12, 0x81, v2
	v_cmp_gt_u32_e32 vcc, s13, v12
	ds_read2_b32 v[12:13], v65 offset0:162 offset1:163
	s_waitcnt lgkmcnt(0)
	v_fmamk_f32 v12, v14, 0x3e38aa3b, v12
	v_add_u32_e32 v14, 0x82, v2
	v_cndmask_b32_e32 v98, v44, v17, vcc
	v_cmp_gt_u32_e32 vcc, s13, v14
	v_add_u32_e32 v2, 0x83, v2
	v_fmac_f32_e32 v13, 0x3e38aa3b, v15
	v_cndmask_b32_e32 v99, v44, v12, vcc
	v_cmp_gt_u32_e32 vcc, s13, v2
	v_max3_f32 v16, v18, v97, v98
	s_nop 0
	v_cndmask_b32_e32 v44, v44, v13, vcc
	v_max3_f32 v2, v16, v99, v44
	v_mov_b32_e32 v12, v2
	s_nop 1
	v_permlane16_swap_b32_e32 v12, v2
	s_and_b64 vcc, exec, s[4:5]
	s_waitcnt lgkmcnt(0)
	v_max_f32_e32 v12, v12, v12
	v_max_f32_e32 v2, v2, v12
	v_mov_b32_e32 v12, v2
	s_nop 1
	v_permlane32_swap_b32_e32 v12, v2
	s_waitcnt lgkmcnt(0)
	v_max_f32_e32 v12, v12, v12
	v_max_f32_e32 v28, v2, v12
	v_sub_f32_e32 v1, v1, v28
	v_sub_f32_e32 v0, v0, v28
	v_exp_f32_e32 v12, v1
	v_sub_f32_e32 v1, v45, v28
	v_sub_f32_e32 v2, v46, v28
	v_exp_f32_e32 v0, v0
	v_exp_f32_e32 v1, v1
	v_exp_f32_e32 v13, v2
	v_cvt_pk_bf16_f32 v24, v0, v12
	v_pk_add_f32 v[14:15], v[0:1], v[12:13]
	v_cvt_pk_bf16_f32 v25, v1, v13
	v_sub_f32_e32 v1, v41, v28
	v_sub_f32_e32 v0, v40, v28
	v_exp_f32_e32 v2, v1
	v_sub_f32_e32 v1, v42, v28
	v_pk_add_f32 v[14:15], v[14:15], v[14:15] op_sel_hi:[0,1]
	v_exp_f32_e32 v0, v0
	v_exp_f32_e32 v12, v1
	v_sub_f32_e32 v1, v43, v28
	v_exp_f32_e32 v14, v1
	v_add_f32_e32 v1, v0, v2
	v_cvt_pk_bf16_f32 v26, v0, v2
	v_sub_f32_e32 v2, v37, v28
	v_add_f32_e32 v13, v12, v14
	v_cvt_pk_bf16_f32 v27, v12, v14
	v_sub_f32_e32 v0, v36, v28
	v_exp_f32_e32 v12, v2
	v_sub_f32_e32 v2, v38, v28
	v_exp_f32_e32 v0, v0
	v_exp_f32_e32 v14, v2
	v_sub_f32_e32 v2, v39, v28
	v_exp_f32_e32 v2, v2
	v_pk_add_f32 v[16:17], v[0:1], v[12:13]
	v_sub_f32_e32 v1, v33, v28
	v_cvt_pk_bf16_f32 v20, v0, v12
	v_pk_add_f32 v[18:19], v[14:15], v[2:3]
	v_cvt_pk_bf16_f32 v21, v14, v2
	v_sub_f32_e32 v0, v32, v28
	v_exp_f32_e32 v12, v1
	v_sub_f32_e32 v1, v47, v28
	v_sub_f32_e32 v2, v35, v28
	v_exp_f32_e32 v0, v0
	v_exp_f32_e32 v1, v1
	v_exp_f32_e32 v13, v2
	v_pk_add_f32 v[16:17], v[16:17], v[18:19]
	v_cvt_pk_bf16_f32 v22, v0, v12
	v_pk_add_f32 v[36:37], v[16:17], v[16:17] op_sel_hi:[0,1]
	v_pk_add_f32 v[14:15], v[0:1], v[12:13]
	v_cvt_pk_bf16_f32 v23, v1, v13
	v_sub_f32_e32 v1, v29, v28
	v_sub_f32_e32 v0, v34, v28
	v_exp_f32_e32 v2, v1
	v_sub_f32_e32 v1, v30, v28
	v_pk_add_f32 v[14:15], v[14:15], v[14:15] op_sel_hi:[0,1]
	v_exp_f32_e32 v0, v0
	v_exp_f32_e32 v12, v1
	v_sub_f32_e32 v1, v31, v28
	v_exp_f32_e32 v14, v1
	v_add_f32_e32 v1, v0, v2
	v_cvt_pk_bf16_f32 v16, v0, v2
	v_sub_f32_e32 v2, v86, v28
	v_add_f32_e32 v13, v12, v14
	v_cvt_pk_bf16_f32 v17, v12, v14
	v_exp_f32_e32 v12, v2
	v_sub_f32_e32 v2, v89, v28
	v_sub_f32_e32 v0, v85, v28
	v_exp_f32_e32 v14, v2
	v_sub_f32_e32 v2, v90, v28
	v_exp_f32_e32 v0, v0
	v_exp_f32_e32 v36, v2
	v_sub_f32_e32 v2, v92, v28
	v_add_u32_e32 v85, s1, v81
	v_pk_add_f32 v[18:19], v[0:1], v[12:13]
	v_pk_add_f32 v[30:31], v[14:15], v[36:37]
	v_sub_f32_e32 v1, v88, v28
	v_pk_add_f32 v[18:19], v[18:19], v[30:31]
	v_exp_f32_e32 v13, v2
	v_pk_add_f32 v[30:31], v[18:19], v[18:19] op_sel_hi:[0,1]
	v_cvt_pk_bf16_f32 v18, v0, v12
	v_sub_f32_e32 v0, v87, v28
	v_exp_f32_e32 v12, v1
	v_sub_f32_e32 v1, v91, v28
	v_exp_f32_e32 v0, v0
	v_exp_f32_e32 v1, v1
	v_cvt_pk_bf16_f32 v19, v14, v36
	v_add_u32_e32 v86, s1, v80
	v_add_u32_e32 v87, s1, v79
	v_pk_add_f32 v[14:15], v[0:1], v[12:13]
	v_cvt_pk_bf16_f32 v12, v0, v12
	v_cvt_pk_bf16_f32 v13, v1, v13
	v_sub_f32_e32 v0, v93, v28
	v_sub_f32_e32 v1, v94, v28
	v_exp_f32_e32 v0, v0
	v_exp_f32_e32 v2, v1
	v_sub_f32_e32 v1, v95, v28
	v_pk_add_f32 v[32:33], v[14:15], v[14:15] op_sel_hi:[0,1]
	v_exp_f32_e32 v15, v1
	v_sub_f32_e32 v1, v96, v28
	v_exp_f32_e32 v29, v1
	v_add_f32_e32 v1, v0, v2
	v_cvt_pk_bf16_f32 v14, v0, v2
	v_sub_f32_e32 v2, v98, v28
	v_exp_f32_e32 v34, v2
	v_sub_f32_e32 v2, v99, v28
	v_exp_f32_e32 v32, v2
	v_sub_f32_e32 v2, v44, v28
	v_exp_f32_e32 v30, v2
	v_sub_f32_e32 v0, v97, v28
	v_exp_f32_e32 v0, v0
	v_add_f32_e32 v35, v15, v29
	v_pk_add_f32 v[38:39], v[32:33], v[30:31]
	v_add_u32_e32 v31, s1, v82
	s_add_i32 s1, s79, s87
	s_add_i32 s1, s1, s0
	s_lshl_b32 s1, s1, 15
	s_and_b32 s1, s1, 0x18000
	s_add_i32 s1, s95, s1
	s_addk_i32 s1, 0x4000
	v_add_u32_e32 v88, s1, v79
	v_add_u32_e32 v89, s1, v80
	v_add_u32_e32 v90, s1, v81
	v_add_u32_e32 v91, s1, v82
	s_add_i32 s1, s82, s87
	s_add_i32 s1, s1, s0
	s_lshl_b32 s1, s1, 15
	s_and_b32 s1, s1, 0x18000
	v_pk_add_f32 v[36:37], v[0:1], v[34:35]
	s_add_i32 s1, s96, s1
	v_pk_add_f32 v[36:37], v[36:37], v[38:39]
	s_addk_i32 s1, 0x4000
	v_cvt_pk_bf16_f32 v15, v15, v29
	v_add_f32_e32 v29, v36, v37
	v_cvt_pk_bf16_f32 v0, v0, v34
	v_cvt_pk_bf16_f32 v1, v32, v30
	ds_read_b64_tr_b16 v[44:45], v87
	ds_read_b64_tr_b16 v[40:41], v86
	ds_read_b64_tr_b16 v[36:37], v85
	ds_read_b64_tr_b16 v[32:33], v31
	ds_read_b64_tr_b16 v[46:47], v88
	ds_read_b64_tr_b16 v[42:43], v89
	ds_read_b64_tr_b16 v[38:39], v90
	ds_read_b64_tr_b16 v[34:35], v91
	s_waitcnt lgkmcnt(0)
; __device__ __forceinline__ void attn_group_ring(const bf16* QK, const float* bias2g, int ldil, int first, bf16* OACC, float* LSE, LAS unsigned char* lds, const int tid, const int bid, const int G) {
;     ...
; #pragma unroll
;           for (int t = 0; t < 5; ++t) {
;               const int wlo = 16 * wq + 32 * t, whi = wlo + 16;
;               const unsigned blo = (unsigned)(size_t)(lds + ((a + (wlo >> 7)) & 3) * 32768 + 16384 + (wlo & 127) * 128), bhi = (unsigned)(size_t)(lds + ((a + (whi >> 7)) & 3) * 32768 + 16384 + (whi & 127) * 128);
;               v2u l0, l1, l2, l3, h0 = (v2u){0u, 0u}, h1 = h0, h2 = h0, h3 = h0;
;               const unsigned a0 = blo + pcs[0], a1 = blo + pcs[1], a2 = blo + pcs[2], a3 = blo + pcs[3];
;               if (t < 4) { const unsigned c0 = bhi + pcs[0], c1 = bhi + pcs[1], c2 = bhi + pcs[2], c3 = bhi + pcs[3];
;                   asm volatile("ds_read_b64_tr_b16 %0, %8\n\tds_read_b64_tr_b16 %1, %9\n\tds_read_b64_tr_b16 %2, %10\n\tds_read_b64_tr_b16 %3, %11\n\t"
;                                "ds_read_b64_tr_b16 %4, %12\n\tds_read_b64_tr_b16 %5, %13\n\tds_read_b64_tr_b16 %6, %14\n\tds_read_b64_tr_b16 %7, %15\n\ts_waitcnt lgkmcnt(0)"
;                                : "=&v"(l0), "=&v"(l1), "=&v"(l2), "=&v"(l3), "=&v"(h0), "=&v"(h1), "=&v"(h2), "=&v"(h3) : "v"(a0), "v"(a1), "v"(a2), "v"(a3), "v"(c0), "v"(c1), "v"(c2), "v"(c3) : "memory"); }
;               else asm volatile("ds_read_b64_tr_b16 %0, %4\n\tds_read_b64_tr_b16 %1, %5\n\tds_read_b64_tr_b16 %2, %6\n\tds_read_b64_tr_b16 %3, %7\n\ts_waitcnt lgkmcnt(0)"
;                                 : "=&v"(l0), "=&v"(l1), "=&v"(l2), "=&v"(l3) : "v"(a0), "v"(a1), "v"(a2), "v"(a3) : "memory");
;               const bf16x8s pf = __builtin_bit_cast(bf16x8s, pb[t]);
;               O[0] = __builtin_amdgcn_mfma_f32_16x16x32_bf16(__builtin_bit_cast(bf16x8s, ((v4u){l0.x, l0.y, h0.x, h0.y})), pf, O[0], 0, 0, 0);
;               O[1] = __builtin_amdgcn_mfma_f32_16x16x32_bf16(__builtin_bit_cast(bf16x8s, ((v4u){l1.x, l1.y, h1.x, h1.y})), pf, O[1], 0, 0, 0);
;               O[2] = __builtin_amdgcn_mfma_f32_16x16x32_bf16(__builtin_bit_cast(bf16x8s, ((v4u){l2.x, l2.y, h2.x, h2.y})), pf, O[2], 0, 0, 0);
;               O[3] = __builtin_amdgcn_mfma_f32_16x16x32_bf16(__builtin_bit_cast(bf16x8s, ((v4u){l3.x, l3.y, h3.x, h3.y})), pf, O[3], 0, 0, 0); } }
	v_add_u32_e32 v31, s1, v82
	v_add_u32_e32 v85, s1, v81
	v_add_u32_e32 v98, s1, v80
	v_add_u32_e32 v99, s1, v79
	s_add_i32 s1, s83, s87
	s_add_i32 s1, s1, s0
	s_lshl_b32 s1, s1, 15
	s_and_b32 s1, s1, 0x18000
	s_add_i32 s1, s97, s1
	s_addk_i32 s1, 0x4000
	v_add_u32_e32 v100, s1, v79
	v_add_u32_e32 v101, s1, v80
	v_add_u32_e32 v102, s1, v81
	v_add_u32_e32 v103, s1, v82
	s_add_i32 s1, s84, s87
	s_add_i32 s1, s1, s0
	v_mfma_f32_16x16x32_bf16 v[44:47], v[44:47], v[24:27], 0
	s_lshl_b32 s1, s1, 15
	s_and_b32 s1, s1, 0x18000
	s_add_i32 s1, s58, s1
	v_mfma_f32_16x16x32_bf16 v[40:43], v[40:43], v[24:27], 0
	s_addk_i32 s1, 0x4000
	v_mov_b32_e32 v2, v3
	v_mov_b32_e32 v30, v29
	s_nop 1
	v_permlane16_swap_b32_e32 v30, v29
	v_mfma_f32_16x16x32_bf16 v[36:39], v[36:39], v[24:27], 0
	s_waitcnt lgkmcnt(0)
	v_add_f32_e32 v29, v29, v30
	v_mfma_f32_16x16x32_bf16 v[24:27], v[32:35], v[24:27], 0
	ds_read_b64_tr_b16 v[94:95], v99
	ds_read_b64_tr_b16 v[90:91], v98
	ds_read_b64_tr_b16 v[86:87], v85
	ds_read_b64_tr_b16 v[32:33], v31
	ds_read_b64_tr_b16 v[96:97], v100
	ds_read_b64_tr_b16 v[92:93], v101
	ds_read_b64_tr_b16 v[88:89], v102
	ds_read_b64_tr_b16 v[34:35], v103
	s_waitcnt lgkmcnt(0)
	v_add_u32_e32 v31, s1, v82
	v_add_u32_e32 v85, s1, v81
	v_mfma_f32_16x16x32_bf16 v[44:47], v[94:97], v[20:23], v[44:47]
	v_add_u32_e32 v94, s1, v80
	v_add_u32_e32 v95, s1, v79
	s_add_i32 s1, s85, s87
	s_add_i32 s1, s1, s0
	s_lshl_b32 s1, s1, 15
	s_and_b32 s1, s1, 0x18000
	s_add_i32 s1, s59, s1
	s_addk_i32 s1, 0x4000
	v_add_u32_e32 v96, s1, v79
	v_add_u32_e32 v97, s1, v80
	v_add_u32_e32 v98, s1, v81
	v_add_u32_e32 v99, s1, v82
	s_add_i32 s1, s86, s87
	s_add_i32 s1, s1, s0
	s_lshl_b32 s1, s1, 15
	s_and_b32 s1, s1, 0x18000
	s_add_i32 s1, s38, s1
	v_mfma_f32_16x16x32_bf16 v[40:43], v[90:93], v[20:23], v[40:43]
	s_addk_i32 s1, 0x4000
	v_mov_b32_e32 v30, v29
	s_nop 1
	v_permlane32_swap_b32_e32 v30, v29
	v_mfma_f32_16x16x32_bf16 v[36:39], v[86:89], v[20:23], v[36:39]
	v_mfma_f32_16x16x32_bf16 v[20:23], v[32:35], v[20:23], v[24:27]
	ds_read_b64_tr_b16 v[90:91], v95
	ds_read_b64_tr_b16 v[86:87], v94
	ds_read_b64_tr_b16 v[32:33], v85
	ds_read_b64_tr_b16 v[24:25], v31
	ds_read_b64_tr_b16 v[92:93], v96
	ds_read_b64_tr_b16 v[88:89], v97
	ds_read_b64_tr_b16 v[34:35], v98
	ds_read_b64_tr_b16 v[26:27], v99
	s_waitcnt lgkmcnt(0)
	v_add_u32_e32 v31, s1, v82
	v_add_u32_e32 v85, s1, v81
	v_mfma_f32_16x16x32_bf16 v[44:47], v[90:93], v[16:19], v[44:47]
	v_add_u32_e32 v90, s1, v80
	v_add_u32_e32 v91, s1, v79
	s_add_i32 s1, s89, s87
	s_add_i32 s1, s1, s0
	s_lshl_b32 s1, s1, 15
	s_and_b32 s1, s1, 0x18000
	s_add_i32 s1, s40, s1
	s_addk_i32 s1, 0x4000
	v_add_u32_e32 v92, s1, v79
	v_add_u32_e32 v93, s1, v80
	v_add_u32_e32 v94, s1, v81
	v_add_u32_e32 v95, s1, v82
	s_add_i32 s1, s91, s87
	s_add_i32 s1, s1, s0
	v_mfma_f32_16x16x32_bf16 v[40:43], v[86:89], v[16:19], v[40:43]
	s_lshl_b32 s0, s1, 15
	s_and_b32 s0, s0, 0x18000
	s_add_i32 s0, s93, s0
	v_mfma_f32_16x16x32_bf16 v[32:35], v[32:35], v[16:19], v[36:39]
	s_addk_i32 s0, 0x4000
	v_mfma_f32_16x16x32_bf16 v[16:19], v[24:27], v[16:19], v[20:23]
	ds_read_b64_tr_b16 v[86:87], v91
	ds_read_b64_tr_b16 v[36:37], v90
	ds_read_b64_tr_b16 v[24:25], v85
	ds_read_b64_tr_b16 v[20:21], v31
	ds_read_b64_tr_b16 v[88:89], v92
	ds_read_b64_tr_b16 v[38:39], v93
	ds_read_b64_tr_b16 v[26:27], v94
	ds_read_b64_tr_b16 v[22:23], v95
	s_waitcnt lgkmcnt(0)
	s_nop 0
	v_mfma_f32_16x16x32_bf16 v[44:47], v[86:89], v[12:15], v[44:47]
	v_mfma_f32_16x16x32_bf16 v[36:39], v[36:39], v[12:15], v[40:43]
	v_mfma_f32_16x16x32_bf16 v[32:35], v[24:27], v[12:15], v[32:35]
	v_add_u32_e32 v24, s0, v80
	v_add_u32_e32 v25, s0, v79
	v_mov_b32_e32 v42, v3
	v_mfma_f32_16x16x32_bf16 v[12:15], v[20:23], v[12:15], v[16:19]
	v_add_u32_e32 v22, s0, v82
	v_add_u32_e32 v23, s0, v81
	ds_read_b64_tr_b16 v[20:21], v25
	ds_read_b64_tr_b16 v[18:19], v24
	ds_read_b64_tr_b16 v[16:17], v23
	ds_read_b64_tr_b16 v[40:41], v22
	s_waitcnt lgkmcnt(0)
	v_mov_b32_e32 v22, v3
	v_mov_b32_e32 v23, v3
	v_mov_b32_e32 v43, v3
	s_nop 0
	v_mfma_f32_16x16x32_bf16 v[24:27], v[20:23], v[0:3], v[44:47]
	v_mov_b32_e32 v20, v3
	v_mov_b32_e32 v21, v3
	v_mfma_f32_16x16x32_bf16 v[12:15], v[40:43], v[0:3], v[12:15]
	s_nop 0
	v_mfma_f32_16x16x32_bf16 v[20:23], v[18:21], v[0:3], v[36:39]
	v_mov_b32_e32 v18, v3
	v_mov_b32_e32 v19, v3
	s_nop 1
	v_mfma_f32_16x16x32_bf16 v[16:19], v[16:19], v[0:3], v[32:35]
	s_waitcnt lgkmcnt(0)
	v_add_f32_e32 v1, v29, v30
	v_rcp_f32_e32 v0, v1
	v_log_f32_e32 v1, v1
	v_mov_b32_e32 v2, 0
	v_add_f32_e32 v28, v28, v1
	s_cbranch_vccnz .LBB0_245
	v_max_f32_e32 v1, v28, v28
	s_waitcnt vmcnt(0)
	ds_bpermute_b32 v84, v116, v84
	s_waitcnt lgkmcnt(0)
	v_max_f32_e32 v2, v84, v84
	v_max_f32_e32 v2, v2, v1
	v_sub_f32_e32 v1, v84, v2
	v_sub_f32_e32 v28, v28, v2
	v_exp_f32_e32 v1, v1
	v_exp_f32_e32 v28, v28
	s_nop 0
	v_add_f32_e32 v30, v1, v28
	v_rcp_f32_e32 v29, v30
	v_log_f32_e32 v30, v30
	v_mul_f32_e32 v28, v28, v29
	v_pk_mul_f32 v[0:1], v[0:1], v[28:29]
	v_add_f32_e32 v28, v2, v30
	v_mov_b32_e32 v2, v1
